# v25 + latent-attention loops use one workgroup barrier per half-step (second one only ordered the ALiBi position row of the window mode)
# speedup vs baseline: 1.0124x; 1.0124x over previous
; template <int MODE>
; __device__ __forceinline__ void partialSM(f32x16& p0, f32x16& p1, float& m_reg, float& mn, float& alpha) {
;     ...
;     const float mnL = -mn * C2;
; #pragma unroll
;     for (int r = 0; r < 16; ++r) p0[r] = fmaf(p0[r], C2, mnL);
; #pragma unroll
;     for (int r = 0; r < 16; ++r) p1[r] = fmaf(p1[r], C2, mnL);
; #pragma unroll
;     for (int r = 0; r < 16; ++r) p0[r] = __builtin_amdgcn_exp2f(p0[r]);
; }
; template <int KB, bool SK, bool ROPE, bool QHALF>
; __device__ __forceinline__ void qkt(f32x16& p0, f32x16& p1, const char* lds, int r32, int hi, const bf16x8* qr, const char* qrl, bool act) {
;     ...
;     const char* kb[4];
; #pragma unroll
;     for (int dd = 0; dd < 4; ++dd) kb[dd] = lds + OFF_K + KB * SHM_K + KSWZ(r32, (dd * 16 + hi * 8) * 2);
; #pragma unroll
;     for (int d0 = 0; d0 < 8; ++d0) { const char* a = kb[d0 & 3] + (d0 >> 2) * 128;
;         bf16x8 b0 = *reinterpret_cast<const bf16x8*>(a);
;         bf16x8 b1 = *reinterpret_cast<const bf16x8*>(a + 32 * 256);
;         bf16x8 qf;
;         if constexpr (QHALF) { if (d0 >= 4) qf = *reinterpret_cast<const bf16x8*>(qrl + (d0 - 4) * 1024); else qf = qr[d0]; } else qf = qr[d0];
;         p0 = __builtin_amdgcn_mfma_f32_32x32x16_bf16(b0, qf, p0, 0, 0, 0);
;         p1 = __builtin_amdgcn_mfma_f32_32x32x16_bf16(b1, qf, p1, 0, 0, 0); }
;     if constexpr (ROPE) {
; #pragma unroll
;         for (int d0 = 0; d0 < 4; ++d0) { const char* a = lds + OFF_KR + KB * SHM_KR + KRSWZ(r32, 2 * d0 + hi);
;             bf16x8 b0 = *reinterpret_cast<const bf16x8*>(a);
;             bf16x8 b1 = *reinterpret_cast<const bf16x8*>(a + 32 * 128);
;             const bf16x8 qf = *reinterpret_cast<const bf16x8*>(qrl + d0 * 1024);
;             p0 = __builtin_amdgcn_mfma_f32_32x32x16_bf16(b0, qf, p0, 0, 0, 0);
;             p1 = __builtin_amdgcn_mfma_f32_32x32x16_bf16(b1, qf, p1, 0, 0, 0); }
.LBB0_524:
	v_cndmask_b32_e64 v178, v5, v228, s[6:7]
	v_mul_f32_e32 v6, 0xbdd53b94, v178
	v_fmamk_f32 v13, v137, 0x3dd53b94, v6
	v_fmamk_f32 v137, v141, 0x3dd53b94, v6
	v_mov_b32_e32 v141, v6
	v_fmamk_f32 v5, v130, 0x3dd53b94, v6
	v_fmamk_f32 v7, v131, 0x3dd53b94, v6
	v_fmamk_f32 v8, v132, 0x3dd53b94, v6
	v_fmamk_f32 v9, v133, 0x3dd53b94, v6
	v_fmamk_f32 v10, v134, 0x3dd53b94, v6
	v_fmamk_f32 v11, v135, 0x3dd53b94, v6
	v_fmamk_f32 v12, v136, 0x3dd53b94, v6
	v_fmamk_f32 v14, v138, 0x3dd53b94, v6
	v_fmamk_f32 v15, v139, 0x3dd53b94, v6
	v_fmamk_f32 v136, v140, 0x3dd53b94, v6
	v_fmamk_f32 v138, v142, 0x3dd53b94, v6
	v_fmamk_f32 v139, v143, 0x3dd53b94, v6
	v_fmamk_f32 v140, v144, 0x3dd53b94, v6
	v_fmac_f32_e32 v141, 0x3dd53b94, v145
	v_exp_f32_e32 v188, v5
	v_exp_f32_e32 v228, v7
	v_exp_f32_e32 v186, v8
	v_exp_f32_e32 v189, v9
	v_exp_f32_e32 v185, v10
	v_exp_f32_e32 v187, v11
	v_exp_f32_e32 v183, v12
	v_exp_f32_e32 v184, v13
	v_exp_f32_e32 v179, v14
	v_exp_f32_e32 v182, v15
	v_exp_f32_e32 v144, v136
	v_exp_f32_e32 v180, v137
	v_exp_f32_e32 v142, v138
	v_exp_f32_e32 v181, v139
	v_exp_f32_e32 v143, v140
	v_exp_f32_e32 v145, v141
	v_add_f32_e32 v5, v195, v226
	v_fmac_f32_e32 v5, v221, v191
	v_add_f32_e32 v191, v229, v230
	s_addk_i32 s48, 0x80
	s_add_i32 s36, s36, 2
	v_pk_fma_f32 v[128:129], v[128:129], s[22:23], v[6:7] op_sel_hi:[1,0,0]
	v_pk_fma_f32 v[126:127], v[126:127], s[22:23], v[6:7] op_sel_hi:[1,0,0]
	v_pk_fma_f32 v[130:131], v[124:125], s[22:23], v[6:7] op_sel_hi:[1,0,0]
	v_pk_fma_f32 v[132:133], v[122:123], s[22:23], v[6:7] op_sel_hi:[1,0,0]
	v_pk_fma_f32 v[134:135], v[120:121], s[22:23], v[6:7] op_sel_hi:[1,0,0]
	v_pk_fma_f32 v[136:137], v[118:119], s[22:23], v[6:7] op_sel_hi:[1,0,0]
	v_pk_fma_f32 v[138:139], v[116:117], s[22:23], v[6:7] op_sel_hi:[1,0,0]
	v_pk_fma_f32 v[140:141], v[114:115], s[22:23], v[6:7] op_sel_hi:[1,0,0]
	v_fmac_f32_e32 v191, v5, v227
	s_cmp_ge_i32 s36, s71
	v_add_u32_e32 v193, 0xffffff80, v193
	v_mov_b32_e32 v221, v4
	s_waitcnt lgkmcnt(0)
	s_cbranch_scc0 .Lmy_nobar_0
	s_barrier
	s_branch .LBB0_541
.Lmy_nobar_0:
.LBB0_525:
	ds_read_b128 v[4:7], v213 offset:49152
	ds_read_b128 v[8:11], v213 offset:57344
	s_add_i32 s10, 0, 0x12800
	v_exp_f32_e32 v122, v132
	v_exp_f32_e32 v123, v133
	s_waitcnt lgkmcnt(1)
	v_mfma_f32_32x32x16_bf16 v[102:117], v[4:7], v[174:177], 0
	v_exp_f32_e32 v124, v130
	v_exp_f32_e32 v125, v131
	v_exp_f32_e32 v126, v126
	v_exp_f32_e32 v127, v127
	v_exp_f32_e32 v128, v128
	v_exp_f32_e32 v129, v129
	s_add_i32 s6, s48, 0xffffff60
	s_waitcnt lgkmcnt(0)
	v_mfma_f32_32x32x16_bf16 v[86:101], v[8:11], v[174:177], 0
	ds_read_b128 v[4:7], v214 offset:49152
	ds_read_b128 v[8:11], v214 offset:57344
	s_add_i32 s7, s48, 0xffffff9f
	s_waitcnt lgkmcnt(1)
	v_mfma_f32_32x32x16_bf16 v[102:117], v[4:7], v[170:173], v[102:117]
	s_waitcnt lgkmcnt(0)
	v_mfma_f32_32x32x16_bf16 v[86:101], v[8:11], v[170:173], v[86:101]
	ds_read_b128 v[4:7], v215 offset:49152
	ds_read_b128 v[8:11], v215 offset:57344
	s_waitcnt lgkmcnt(1)
	v_mfma_f32_32x32x16_bf16 v[102:117], v[4:7], v[166:169], v[102:117]
	s_waitcnt lgkmcnt(0)
	v_mfma_f32_32x32x16_bf16 v[86:101], v[8:11], v[166:169], v[86:101]
	ds_read_b128 v[4:7], v216 offset:49152
	ds_read_b128 v[8:11], v216 offset:57344
	s_waitcnt lgkmcnt(1)
	v_mfma_f32_32x32x16_bf16 v[102:117], v[4:7], v[162:165], v[102:117]
	s_waitcnt lgkmcnt(0)
	v_mfma_f32_32x32x16_bf16 v[86:101], v[8:11], v[162:165], v[86:101]
	ds_read_b128 v[4:7], v213 offset:49280
	ds_read_b128 v[8:11], v213 offset:57472
	s_waitcnt lgkmcnt(1)
	v_mfma_f32_32x32x16_bf16 v[102:117], v[4:7], v[158:161], v[102:117]
	s_waitcnt lgkmcnt(0)
	v_mfma_f32_32x32x16_bf16 v[86:101], v[8:11], v[158:161], v[86:101]
	ds_read_b128 v[4:7], v214 offset:49280
	ds_read_b128 v[8:11], v214 offset:57472
	s_waitcnt lgkmcnt(1)
	v_mfma_f32_32x32x16_bf16 v[102:117], v[4:7], v[154:157], v[102:117]
	s_waitcnt lgkmcnt(0)
	v_mfma_f32_32x32x16_bf16 v[86:101], v[8:11], v[154:157], v[86:101]
	ds_read_b128 v[4:7], v215 offset:49280
	ds_read_b128 v[8:11], v215 offset:57472
	s_waitcnt lgkmcnt(1)
	v_mfma_f32_32x32x16_bf16 v[102:117], v[4:7], v[150:153], v[102:117]
	s_waitcnt lgkmcnt(0)
	v_mfma_f32_32x32x16_bf16 v[86:101], v[8:11], v[150:153], v[86:101]
	ds_read_b128 v[4:7], v216 offset:49280
	ds_read_b128 v[8:11], v216 offset:57472
	s_waitcnt lgkmcnt(1)
	v_mfma_f32_32x32x16_bf16 v[102:117], v[4:7], v[146:149], v[102:117]
	s_waitcnt lgkmcnt(0)
	v_mfma_f32_32x32x16_bf16 v[86:101], v[8:11], v[146:149], v[86:101]
	v_add_u32_e32 v8, s10, v217
	ds_read_b128 v[4:7], v8
	ds_read_b128 v[8:11], v8 offset:4096
	ds_read_b128 v[12:15], v202
	s_waitcnt lgkmcnt(0)
	v_mfma_f32_32x32x16_bf16 v[102:117], v[4:7], v[12:15], v[102:117]
	v_mfma_f32_32x32x16_bf16 v[86:101], v[8:11], v[12:15], v[86:101]
	v_add_u32_e32 v8, s10, v218
	ds_read_b128 v[4:7], v8
	ds_read_b128 v[8:11], v8 offset:4096
	ds_read_b128 v[12:15], v202 offset:1024
	s_waitcnt lgkmcnt(0)
	v_mfma_f32_32x32x16_bf16 v[102:117], v[4:7], v[12:15], v[102:117]
	v_mfma_f32_32x32x16_bf16 v[86:101], v[8:11], v[12:15], v[86:101]
	v_add_u32_e32 v8, s10, v219
	ds_read_b128 v[4:7], v8
	ds_read_b128 v[8:11], v8 offset:4096
	ds_read_b128 v[12:15], v202 offset:2048
	s_waitcnt lgkmcnt(0)
	v_mfma_f32_32x32x16_bf16 v[102:117], v[4:7], v[12:15], v[102:117]
	v_mfma_f32_32x32x16_bf16 v[86:101], v[8:11], v[12:15], v[86:101]
	v_add_u32_e32 v8, s10, v220
	ds_read_b128 v[4:7], v8
	ds_read_b128 v[8:11], v8 offset:4096
	ds_read_b128 v[12:15], v202 offset:3072
	s_waitcnt lgkmcnt(0)
; __device__ __forceinline__ void finishSM(f32x16& p0, f32x16& p1, float alpha, float& l_reg, bf16x8& pa0, bf16x8& pa1, bf16x8& pa2, bf16x8& pa3) {
; #pragma unroll
;     for (int r = 0; r < 16; ++r) p1[r] = __builtin_amdgcn_exp2f(p1[r]);
;     float ps = 0;
; #pragma unroll
;     for (int r = 0; r < 16; ++r) ps += p0[r];
; #pragma unroll
;     for (int r = 0; r < 16; ++r) ps += p1[r];
;     { auto rr = __builtin_amdgcn_permlane32_swap(__float_as_uint(ps), __float_as_uint(ps), false, false);
;       ps = __uint_as_float(rr[0]) + __uint_as_float(rr[1]); }
;     l_reg = l_reg * alpha + ps;
;     ...
;     PK4(p0, 0, pa0); PK4(p0, 8, pa1); PK4(p1, 0, pa2); PK4(p1, 8, pa3);
;     ...
; }
; template <int VB, bool SK>
; __device__ __forceinline__ void pv_tile(f32x16* o, int vb0, bf16x8 pa0, bf16x8 pa1, bf16x8 pa2, bf16x8 pa3, bool act) {
;     if (SK && !act) return;
;     ...
;     if (ATT_PRIO) __builtin_amdgcn_s_setprio(1);
;     PV_D0(0); PV_D0(1); PV_D0(2); PV_D0(3);
	v_mfma_f32_32x32x16_bf16 v[102:117], v[4:7], v[12:15], v[102:117]
	v_exp_f32_e32 v4, v140
	v_exp_f32_e32 v5, v141
	v_exp_f32_e32 v6, v138
	v_exp_f32_e32 v7, v139
	v_mfma_f32_32x32x16_bf16 v[86:101], v[8:11], v[12:15], v[86:101]
	v_add_f32_e32 v12, 0, v188
	v_add_f32_e32 v12, v228, v12
	v_add_f32_e32 v12, v186, v12
	v_add_f32_e32 v12, v189, v12
	v_add_f32_e32 v12, v185, v12
	v_add_f32_e32 v12, v187, v12
	v_add_f32_e32 v12, v183, v12
	v_add_f32_e32 v12, v184, v12
	v_add_f32_e32 v12, v179, v12
	v_add_f32_e32 v12, v182, v12
	v_add_f32_e32 v12, v144, v12
	v_add_f32_e32 v12, v180, v12
	v_add_f32_e32 v12, v142, v12
	v_add_f32_e32 v12, v181, v12
	v_add_f32_e32 v12, v143, v12
	v_add_f32_e32 v12, v145, v12
	v_exp_f32_e32 v8, v136
	v_add_f32_e32 v12, v4, v12
	v_exp_f32_e32 v9, v137
	v_add_f32_e32 v12, v5, v12
	v_exp_f32_e32 v10, v134
	v_add_f32_e32 v12, v6, v12
	v_exp_f32_e32 v11, v135
	v_add_f32_e32 v12, v7, v12
	v_add_f32_e32 v12, v8, v12
	v_add_f32_e32 v12, v9, v12
	v_add_f32_e32 v12, v10, v12
	v_add_f32_e32 v12, v11, v12
	v_add_f32_e32 v12, v122, v12
	v_add_f32_e32 v12, v123, v12
	v_add_f32_e32 v12, v124, v12
	v_add_f32_e32 v12, v125, v12
	v_add_f32_e32 v12, v126, v12
	v_add_f32_e32 v12, v127, v12
	v_add_f32_e32 v12, v128, v12
	v_add_f32_e32 v195, v129, v12
	v_mov_b32_e32 v226, v195
	s_nop 1
	v_permlane32_swap_b32_e32 v195, v226
	v_cvt_pk_bf16_f32 v12, v188, v228
	v_cvt_pk_bf16_f32 v13, v186, v189
	v_cvt_pk_bf16_f32 v14, v185, v187
	v_cvt_pk_bf16_f32 v15, v183, v184
	v_cvt_pk_bf16_f32 v82, v179, v182
	v_cvt_pk_bf16_f32 v83, v144, v180
	v_cvt_pk_bf16_f32 v84, v142, v181
	v_cvt_pk_bf16_f32 v85, v143, v145
	v_cvt_pk_bf16_f32 v118, v4, v5
	v_cvt_pk_bf16_f32 v119, v6, v7
	v_cvt_pk_bf16_f32 v120, v8, v9
	v_cvt_pk_bf16_f32 v121, v10, v11
	v_cvt_pk_bf16_f32 v122, v122, v123
	v_cvt_pk_bf16_f32 v123, v124, v125
	v_cvt_pk_bf16_f32 v124, v126, v127
	v_cvt_pk_bf16_f32 v125, v128, v129
	s_nop 0
	v_permlane32_swap_b32_e32 v12, v14
	v_permlane32_swap_b32_e32 v13, v15
	v_permlane32_swap_b32_e32 v82, v84
	v_permlane32_swap_b32_e32 v83, v85
	v_permlane32_swap_b32_e32 v118, v120
	v_permlane32_swap_b32_e32 v119, v121
	v_permlane32_swap_b32_e32 v122, v124
	v_permlane32_swap_b32_e32 v123, v125
	s_add_i32 s10, s48, 0xffffffa0
	s_sub_i32 s72, s48, 64
	s_mov_b32 s73, s11
	s_lshl_b64 s[50:51], s[10:11], 12
	s_lshl_b64 s[72:73], s[72:73], 12
	v_lshl_add_u64 v[4:5], v[196:197], 0, s[50:51]
	v_lshl_add_u64 v[8:9], v[196:197], 0, s[72:73]
	v_lshl_add_u64 v[126:127], v[198:199], 0, s[50:51]
	s_add_i32 m0, s37, 0x8000
	global_load_dwordx4 v[4:7], v[4:5], off
	s_nop 0
	global_load_dwordx4 v[8:11], v[8:9], off
	s_lshl_b64 s[50:51], s[10:11], 7
	global_load_lds_dwordx4 v[126:127], off
	v_lshl_add_u64 v[126:127], v[198:199], 0, s[72:73]
	s_add_i32 m0, s37, 0xa000
	s_nop 0
	global_load_lds_dwordx4 v[126:127], off
	v_lshl_add_u64 v[126:127], v[16:17], 0, s[50:51]
	s_add_i32 m0, s37, 0x10800
	s_nop 0
	global_load_lds_dwordx4 v[126:127], off
	ds_read_b64_tr_b16 v[126:127], v210 offset:0
	ds_read_b64_tr_b16 v[128:129], v210 offset:0x800
	ds_read_b64_tr_b16 v[130:131], v210 offset:0x1000
	ds_read_b64_tr_b16 v[132:133], v210 offset:0x1800
	ds_read_b64_tr_b16 v[134:135], v210 offset:0x2000
	ds_read_b64_tr_b16 v[136:137], v210 offset:0x2800
	ds_read_b64_tr_b16 v[138:139], v210 offset:0x3000
	ds_read_b64_tr_b16 v[140:141], v210 offset:0x3800
	s_waitcnt lgkmcnt(0)
	s_nop 0
	v_mfma_f32_32x32x16_bf16 v[66:81], v[12:15], v[126:129], v[66:81]
	ds_read_b64_tr_b16 v[126:127], v210 offset:0x200
	ds_read_b64_tr_b16 v[128:129], v210 offset:0xa00
	v_mfma_f32_32x32x16_bf16 v[66:81], v[82:85], v[130:133], v[66:81]
	ds_read_b64_tr_b16 v[130:131], v210 offset:0x1200
	ds_read_b64_tr_b16 v[132:133], v210 offset:0x1a00
	v_mfma_f32_32x32x16_bf16 v[66:81], v[118:121], v[134:137], v[66:81]
	ds_read_b64_tr_b16 v[134:135], v210 offset:0x2200
	ds_read_b64_tr_b16 v[136:137], v210 offset:0x2a00
	ds_read_b64_tr_b16 v[142:143], v210 offset:0x3200
	ds_read_b64_tr_b16 v[144:145], v210 offset:0x3a00
	s_waitcnt lgkmcnt(0)
	v_mfma_f32_32x32x16_bf16 v[66:81], v[122:125], v[138:141], v[66:81]
	v_mfma_f32_32x32x16_bf16 v[50:65], v[12:15], v[126:129], v[50:65]
	ds_read_b64_tr_b16 v[126:127], v210 offset:0x400
	ds_read_b64_tr_b16 v[128:129], v210 offset:0xc00
	v_mfma_f32_32x32x16_bf16 v[50:65], v[82:85], v[130:133], v[50:65]
	ds_read_b64_tr_b16 v[130:131], v210 offset:0x1400
	ds_read_b64_tr_b16 v[132:133], v210 offset:0x1c00
	v_mfma_f32_32x32x16_bf16 v[50:65], v[118:121], v[134:137], v[50:65]
	ds_read_b64_tr_b16 v[134:135], v210 offset:0x2400
	ds_read_b64_tr_b16 v[136:137], v210 offset:0x2c00
	ds_read_b64_tr_b16 v[138:139], v210 offset:0x3400
	ds_read_b64_tr_b16 v[140:141], v210 offset:0x3c00
	s_waitcnt lgkmcnt(0)
	v_mfma_f32_32x32x16_bf16 v[50:65], v[122:125], v[142:145], v[50:65]
	v_mfma_f32_32x32x16_bf16 v[34:49], v[12:15], v[126:129], v[34:49]
	ds_read_b64_tr_b16 v[126:127], v210 offset:0x600
	ds_read_b64_tr_b16 v[128:129], v210 offset:0xe00
	v_mfma_f32_32x32x16_bf16 v[34:49], v[82:85], v[130:133], v[34:49]
	ds_read_b64_tr_b16 v[130:131], v210 offset:0x1600
	ds_read_b64_tr_b16 v[132:133], v210 offset:0x1e00
	v_mfma_f32_32x32x16_bf16 v[34:49], v[118:121], v[134:137], v[34:49]
	ds_read_b64_tr_b16 v[134:135], v210 offset:0x2600
	ds_read_b64_tr_b16 v[136:137], v210 offset:0x2e00
	ds_read_b64_tr_b16 v[142:143], v210 offset:0x3600
	ds_read_b64_tr_b16 v[144:145], v210 offset:0x3e00
	s_waitcnt lgkmcnt(0)
	v_mfma_f32_32x32x16_bf16 v[34:49], v[122:125], v[138:141], v[34:49]
	v_mfma_f32_32x32x16_bf16 v[18:33], v[12:15], v[126:129], v[18:33]
	s_cmp_le_i32 s7, s46
	s_cselect_b64 s[50:51], -1, 0
	s_cmp_gt_i32 s6, s18
	s_cselect_b64 s[6:7], -1, 0
	s_and_b64 s[6:7], s[6:7], s[50:51]
	s_and_b64 vcc, exec, s[6:7]
	v_mfma_f32_32x32x16_bf16 v[18:33], v[82:85], v[130:133], v[18:33]
	v_mfma_f32_32x32x16_bf16 v[18:33], v[118:121], v[134:137], v[18:33]
	v_mfma_f32_32x32x16_bf16 v[18:33], v[122:125], v[142:145], v[18:33]
	s_cbranch_vccnz .LBB0_527
; __device__ __forceinline__ void mask_tile(f32x16& p0, f32x16& p1, int dq, unsigned W) {
;     const float NEG = -__builtin_inff();
; #pragma unroll
;     for (int r = 0; r < 16; ++r) {
;         const int c = (r & 3) + 8 * (r >> 2);
;         if ((unsigned)(dq - c) >= W) p0[r] = NEG;
;         if ((unsigned)(dq - c - 32) >= W) p1[r] = NEG;
;     }
; }
	v_add_u32_e32 v12, 0x7b, v193
	v_cmp_gt_u32_e32 vcc, 2.0, v12
	v_add_u32_e32 v12, 0x5b, v193
	s_nop 0
	v_cndmask_b32_e32 v102, v200, v102, vcc
	v_cmp_gt_u32_e32 vcc, 2.0, v12
	v_add_u32_e32 v12, 0x7a, v193
	s_nop 0
	v_cndmask_b32_e32 v86, v200, v86, vcc
	v_cmp_gt_u32_e32 vcc, 2.0, v12
	v_add_u32_e32 v12, 0x5a, v193
	s_nop 0
	v_cndmask_b32_e32 v103, v200, v103, vcc
	v_cmp_gt_u32_e32 vcc, 2.0, v12
	v_add_u32_e32 v12, 0x79, v193
	s_nop 0
	v_cndmask_b32_e32 v87, v200, v87, vcc
	v_cmp_gt_u32_e32 vcc, 2.0, v12
	v_add_u32_e32 v12, 0x59, v193
	s_nop 0
	v_cndmask_b32_e32 v104, v200, v104, vcc
	v_cmp_gt_u32_e32 vcc, 2.0, v12
	v_add_u32_e32 v12, 0x78, v193
	s_nop 0
	v_cndmask_b32_e32 v88, v200, v88, vcc
	v_cmp_gt_u32_e32 vcc, 2.0, v12
	v_add_u32_e32 v12, 0x58, v193
	s_nop 0
	v_cndmask_b32_e32 v105, v200, v105, vcc
	v_cmp_gt_u32_e32 vcc, 2.0, v12
	v_add_u32_e32 v12, 0x73, v193
	s_nop 0
	v_cndmask_b32_e32 v89, v200, v89, vcc
	v_cmp_gt_u32_e32 vcc, 2.0, v12
	v_add_u32_e32 v12, 0x53, v193
	s_nop 0
	v_cndmask_b32_e32 v106, v200, v106, vcc
	v_cmp_gt_u32_e32 vcc, 2.0, v12
	v_add_u32_e32 v12, 0x72, v193
	s_nop 0
	v_cndmask_b32_e32 v90, v200, v90, vcc
	v_cmp_gt_u32_e32 vcc, 2.0, v12
	v_add_u32_e32 v12, 0x52, v193
	s_nop 0
	v_cndmask_b32_e32 v107, v200, v107, vcc
	v_cmp_gt_u32_e32 vcc, 2.0, v12
	v_add_u32_e32 v12, 0x71, v193
	s_nop 0
	v_cndmask_b32_e32 v91, v200, v91, vcc
	v_cmp_gt_u32_e32 vcc, 2.0, v12
	v_add_u32_e32 v12, 0x51, v193
	s_nop 0
	v_cndmask_b32_e32 v108, v200, v108, vcc
	v_cmp_gt_u32_e32 vcc, 2.0, v12
	v_add_u32_e32 v12, 0x70, v193
	s_nop 0
	v_cndmask_b32_e32 v92, v200, v92, vcc
	v_cmp_gt_u32_e32 vcc, 2.0, v12
	v_add_u32_e32 v12, 0x50, v193
	s_nop 0
	v_cndmask_b32_e32 v109, v200, v109, vcc
	v_cmp_gt_u32_e32 vcc, 2.0, v12
	v_add_u32_e32 v12, 0x6b, v193
	s_nop 0
	v_cndmask_b32_e32 v93, v200, v93, vcc
	v_cmp_gt_u32_e32 vcc, 2.0, v12
	v_add_u32_e32 v12, 0x4b, v193
	s_nop 0
	v_cndmask_b32_e32 v110, v200, v110, vcc
	v_cmp_gt_u32_e32 vcc, 2.0, v12
	v_add_u32_e32 v12, 0x6a, v193
	s_nop 0
	v_cndmask_b32_e32 v94, v200, v94, vcc
	v_cmp_gt_u32_e32 vcc, 2.0, v12
	v_add_u32_e32 v12, 0x4a, v193
	s_nop 0
	v_cndmask_b32_e32 v111, v200, v111, vcc
	v_cmp_gt_u32_e32 vcc, 2.0, v12
	v_add_u32_e32 v12, 0x69, v193
	s_nop 0
	v_cndmask_b32_e32 v95, v200, v95, vcc
	v_cmp_gt_u32_e32 vcc, 2.0, v12
	v_add_u32_e32 v12, 0x49, v193
	s_nop 0
	v_cndmask_b32_e32 v112, v200, v112, vcc
	v_cmp_gt_u32_e32 vcc, 2.0, v12
	v_add_u32_e32 v12, 0x68, v193
	s_nop 0
	v_cndmask_b32_e32 v96, v200, v96, vcc
	v_cmp_gt_u32_e32 vcc, 2.0, v12
	v_add_u32_e32 v12, 0x48, v193
	s_nop 0
	v_cndmask_b32_e32 v113, v200, v113, vcc
	v_cmp_gt_u32_e32 vcc, 2.0, v12
	v_add_u32_e32 v12, 0x63, v193
	s_nop 0
	v_cndmask_b32_e32 v97, v200, v97, vcc
	v_cmp_gt_u32_e32 vcc, 2.0, v12
	v_add_u32_e32 v12, 0x43, v193
	s_nop 0
	v_cndmask_b32_e32 v114, v200, v114, vcc
	v_cmp_gt_u32_e32 vcc, 2.0, v12
	v_add_u32_e32 v12, 0x62, v193
	s_nop 0
	v_cndmask_b32_e32 v98, v200, v98, vcc
	v_cmp_gt_u32_e32 vcc, 2.0, v12
	v_add_u32_e32 v12, 0x42, v193
	s_nop 0
	v_cndmask_b32_e32 v115, v200, v115, vcc
	v_cmp_gt_u32_e32 vcc, 2.0, v12
	v_add_u32_e32 v12, 0x61, v193
	s_nop 0
	v_cndmask_b32_e32 v99, v200, v99, vcc
	v_cmp_gt_u32_e32 vcc, 2.0, v12
	v_add_u32_e32 v12, 0x41, v193
	s_nop 0
	v_cndmask_b32_e32 v116, v200, v116, vcc
	v_cmp_gt_u32_e32 vcc, 2.0, v12
	v_add_u32_e32 v12, 0x60, v193
	s_nop 0
	v_cndmask_b32_e32 v100, v200, v100, vcc
	v_cmp_gt_u32_e32 vcc, 2.0, v12
	v_add_u32_e32 v12, 64, v193
	s_nop 0
	v_cndmask_b32_e32 v117, v200, v117, vcc
	v_cmp_gt_u32_e32 vcc, 2.0, v12
	s_nop 1
	v_cndmask_b32_e32 v101, v200, v101, vcc

; template <int MODE>
; __device__ __forceinline__ void partialSM(f32x16& p0, f32x16& p1, float& m_reg, float& mn, float& alpha) {
;     ...
;     constexpr float C2 = 1.4426950408889634f * SCALE;
;     if (__builtin_expect(__all((pmax - m_reg) * SCALE <= THR), 1)) { mn = m_reg; alpha = 1.f; }
;     else { mn = fmaxf(m_reg, pmax); alpha = __builtin_amdgcn_exp2f((m_reg - mn) * C2); m_reg = mn; }
;     const float mnL = -mn * C2;
; #pragma unroll
;     for (int r = 0; r < 16; ++r) p0[r] = fmaf(p0[r], C2, mnL);
; #pragma unroll
;     for (int r = 0; r < 16; ++r) p1[r] = fmaf(p1[r], C2, mnL);
; #pragma unroll
;     for (int r = 0; r < 16; ++r) p0[r] = __builtin_amdgcn_exp2f(p0[r]);
; template <int KB, bool SK, bool ROPE, bool QHALF>
; __device__ __forceinline__ void qkt(f32x16& p0, f32x16& p1, const char* lds, int r32, int hi, const bf16x8* qr, const char* qrl, bool act) {
;     ...
;     const char* kb[4];
; #pragma unroll
;     for (int dd = 0; dd < 4; ++dd) kb[dd] = lds + OFF_K + KB * SHM_K + KSWZ(r32, (dd * 16 + hi * 8) * 2);
; #pragma unroll
;     for (int d0 = 0; d0 < 8; ++d0) { const char* a = kb[d0 & 3] + (d0 >> 2) * 128;
;         bf16x8 b0 = *reinterpret_cast<const bf16x8*>(a);
;         bf16x8 b1 = *reinterpret_cast<const bf16x8*>(a + 32 * 256);
;         bf16x8 qf;
;         if constexpr (QHALF) { if (d0 >= 4) qf = *reinterpret_cast<const bf16x8*>(qrl + (d0 - 4) * 1024); else qf = qr[d0]; } else qf = qr[d0];
;         p0 = __builtin_amdgcn_mfma_f32_32x32x16_bf16(b0, qf, p0, 0, 0, 0);
;         p1 = __builtin_amdgcn_mfma_f32_32x32x16_bf16(b1, qf, p1, 0, 0, 0); }
.LBB0_531:
	v_cndmask_b32_e64 v228, v12, v178, s[6:7]
	v_mul_f32_e32 v12, 0xbdd53b94, v228
	v_fmamk_f32 v82, v102, 0x3dd53b94, v12
	v_fmamk_f32 v83, v103, 0x3dd53b94, v12
	v_fmamk_f32 v84, v104, 0x3dd53b94, v12
	v_fmamk_f32 v85, v105, 0x3dd53b94, v12
	v_fmamk_f32 v118, v106, 0x3dd53b94, v12
	v_fmamk_f32 v119, v107, 0x3dd53b94, v12
	v_fmamk_f32 v120, v108, 0x3dd53b94, v12
	v_fmamk_f32 v121, v109, 0x3dd53b94, v12
	v_fmamk_f32 v122, v110, 0x3dd53b94, v12
	v_fmamk_f32 v123, v111, 0x3dd53b94, v12
	v_fmamk_f32 v112, v112, 0x3dd53b94, v12
	v_fmamk_f32 v113, v113, 0x3dd53b94, v12
	v_fmamk_f32 v114, v114, 0x3dd53b94, v12
	v_fmamk_f32 v115, v115, 0x3dd53b94, v12
	v_fmamk_f32 v116, v116, 0x3dd53b94, v12
	v_fmamk_f32 v117, v117, 0x3dd53b94, v12
	v_fmamk_f32 v102, v86, 0x3dd53b94, v12
	v_fmamk_f32 v103, v87, 0x3dd53b94, v12
	v_fmamk_f32 v104, v88, 0x3dd53b94, v12
	v_fmamk_f32 v110, v89, 0x3dd53b94, v12
	v_fmamk_f32 v111, v90, 0x3dd53b94, v12
	v_fmamk_f32 v14, v91, 0x3dd53b94, v12
	v_fmamk_f32 v15, v92, 0x3dd53b94, v12
	v_fmamk_f32 v105, v93, 0x3dd53b94, v12
	v_fmamk_f32 v106, v94, 0x3dd53b94, v12
	v_fmamk_f32 v107, v95, 0x3dd53b94, v12
	v_fmamk_f32 v108, v96, 0x3dd53b94, v12
	v_fmamk_f32 v109, v97, 0x3dd53b94, v12
	v_exp_f32_e32 v82, v82
	v_exp_f32_e32 v83, v83
	v_exp_f32_e32 v84, v84
	v_exp_f32_e32 v85, v85
	v_exp_f32_e32 v86, v118
	v_exp_f32_e32 v87, v119
	v_exp_f32_e32 v88, v120
	v_exp_f32_e32 v89, v121
	v_exp_f32_e32 v90, v122
	v_exp_f32_e32 v91, v123
	v_exp_f32_e32 v92, v112
	v_exp_f32_e32 v93, v113
	v_exp_f32_e32 v94, v114
	v_exp_f32_e32 v95, v115
	v_exp_f32_e32 v96, v116
	v_exp_f32_e32 v97, v117
	v_fmamk_f32 v13, v98, 0x3dd53b94, v12
	v_fmamk_f32 v112, v99, 0x3dd53b94, v12
	v_fmamk_f32 v113, v100, 0x3dd53b94, v12
	v_fmac_f32_e32 v12, 0x3dd53b94, v101
	s_waitcnt lgkmcnt(0)
	ds_read_b128 v[98:101], v213 offset:32768
	ds_read_b128 v[114:117], v213 offset:40960
	v_exp_f32_e32 v105, v105
	v_exp_f32_e32 v106, v106
	v_exp_f32_e32 v107, v107
	s_waitcnt lgkmcnt(1)
	v_mfma_f32_32x32x16_bf16 v[130:145], v[98:101], v[174:177], 0
	ds_read_b128 v[98:101], v214 offset:32768
	ds_read_b128 v[178:181], v214 offset:40960
	v_exp_f32_e32 v108, v108
	v_exp_f32_e32 v109, v109
	s_waitcnt lgkmcnt(2)
	v_mfma_f32_32x32x16_bf16 v[114:129], v[114:117], v[174:177], 0
	s_waitcnt lgkmcnt(1)
	v_mfma_f32_32x32x16_bf16 v[130:145], v[98:101], v[170:173], v[130:145]
	s_waitcnt lgkmcnt(0)
	v_mfma_f32_32x32x16_bf16 v[114:129], v[178:181], v[170:173], v[114:129]
	ds_read_b128 v[98:101], v215 offset:32768
	ds_read_b128 v[178:181], v215 offset:40960
	s_waitcnt lgkmcnt(1)
	v_mfma_f32_32x32x16_bf16 v[130:145], v[98:101], v[166:169], v[130:145]
	s_waitcnt lgkmcnt(0)
	v_mfma_f32_32x32x16_bf16 v[114:129], v[178:181], v[166:169], v[114:129]
	ds_read_b128 v[98:101], v216 offset:32768
	ds_read_b128 v[178:181], v216 offset:40960
	s_waitcnt lgkmcnt(1)
	v_mfma_f32_32x32x16_bf16 v[130:145], v[98:101], v[162:165], v[130:145]
	s_waitcnt lgkmcnt(0)
	v_mfma_f32_32x32x16_bf16 v[114:129], v[178:181], v[162:165], v[114:129]
	ds_read_b128 v[98:101], v213 offset:32896
	ds_read_b128 v[178:181], v213 offset:41088
	s_waitcnt lgkmcnt(1)
	v_mfma_f32_32x32x16_bf16 v[130:145], v[98:101], v[158:161], v[130:145]
	s_waitcnt lgkmcnt(0)
	v_mfma_f32_32x32x16_bf16 v[114:129], v[178:181], v[158:161], v[114:129]
	ds_read_b128 v[98:101], v214 offset:32896
	ds_read_b128 v[178:181], v214 offset:41088
	s_waitcnt lgkmcnt(1)
	v_mfma_f32_32x32x16_bf16 v[130:145], v[98:101], v[154:157], v[130:145]
	s_waitcnt lgkmcnt(0)
	v_mfma_f32_32x32x16_bf16 v[114:129], v[178:181], v[154:157], v[114:129]
	ds_read_b128 v[98:101], v215 offset:32896
	ds_read_b128 v[178:181], v215 offset:41088
	s_waitcnt lgkmcnt(1)
	v_mfma_f32_32x32x16_bf16 v[130:145], v[98:101], v[150:153], v[130:145]
	s_waitcnt lgkmcnt(0)
	v_mfma_f32_32x32x16_bf16 v[114:129], v[178:181], v[150:153], v[114:129]
	ds_read_b128 v[98:101], v216 offset:32896
	ds_read_b128 v[178:181], v216 offset:41088
	s_waitcnt lgkmcnt(1)
	v_mfma_f32_32x32x16_bf16 v[130:145], v[98:101], v[146:149], v[130:145]
	s_waitcnt lgkmcnt(0)
; __device__ __forceinline__ void finishSM(f32x16& p0, f32x16& p1, float alpha, float& l_reg, bf16x8& pa0, bf16x8& pa1, bf16x8& pa2, bf16x8& pa3) {
; #pragma unroll
;     for (int r = 0; r < 16; ++r) p1[r] = __builtin_amdgcn_exp2f(p1[r]);
;     float ps = 0;
; #pragma unroll
;     for (int r = 0; r < 16; ++r) ps += p0[r];
; #pragma unroll
;     for (int r = 0; r < 16; ++r) ps += p1[r];
;     { auto rr = __builtin_amdgcn_permlane32_swap(__float_as_uint(ps), __float_as_uint(ps), false, false);
;       ps = __uint_as_float(rr[0]) + __uint_as_float(rr[1]); }
;     l_reg = l_reg * alpha + ps;
;     ...
;     PK4(p0, 0, pa0); PK4(p0, 8, pa1); PK4(p1, 0, pa2); PK4(p1, 8, pa3);
;     ...
; }
; template <int KB, bool SK, bool ROPE, bool QHALF>
; __device__ __forceinline__ void qkt(f32x16& p0, f32x16& p1, const char* lds, int r32, int hi, const bf16x8* qr, const char* qrl, bool act) {
;     ...
;     if constexpr (ROPE) {
; #pragma unroll
;         for (int d0 = 0; d0 < 4; ++d0) { const char* a = lds + OFF_KR + KB * SHM_KR + KRSWZ(r32, 2 * d0 + hi);
;             bf16x8 b0 = *reinterpret_cast<const bf16x8*>(a);
;             bf16x8 b1 = *reinterpret_cast<const bf16x8*>(a + 32 * 128);
;             const bf16x8 qf = *reinterpret_cast<const bf16x8*>(qrl + d0 * 1024);
;             p0 = __builtin_amdgcn_mfma_f32_32x32x16_bf16(b0, qf, p0, 0, 0, 0);
;             p1 = __builtin_amdgcn_mfma_f32_32x32x16_bf16(b1, qf, p1, 0, 0, 0); }
	v_mfma_f32_32x32x16_bf16 v[114:129], v[178:181], v[146:149], v[114:129]
	ds_read_b128 v[98:101], v222
	ds_read_b128 v[178:181], v222 offset:4096
	ds_read_b128 v[182:185], v202
	s_waitcnt lgkmcnt(0)
	v_mfma_f32_32x32x16_bf16 v[130:145], v[98:101], v[182:185], v[130:145]
	v_mfma_f32_32x32x16_bf16 v[114:129], v[178:181], v[182:185], v[114:129]
	ds_read_b128 v[98:101], v223
	ds_read_b128 v[178:181], v223 offset:4096
	ds_read_b128 v[182:185], v202 offset:1024
	s_waitcnt lgkmcnt(0)
	v_mfma_f32_32x32x16_bf16 v[130:145], v[98:101], v[182:185], v[130:145]
	v_mfma_f32_32x32x16_bf16 v[114:129], v[178:181], v[182:185], v[114:129]
	ds_read_b128 v[98:101], v224
	ds_read_b128 v[178:181], v224 offset:4096
	ds_read_b128 v[182:185], v202 offset:2048
	s_waitcnt lgkmcnt(0)
	v_mfma_f32_32x32x16_bf16 v[130:145], v[98:101], v[182:185], v[130:145]
	v_mfma_f32_32x32x16_bf16 v[114:129], v[178:181], v[182:185], v[114:129]
	ds_read_b128 v[98:101], v225
	ds_read_b128 v[178:181], v225 offset:4096
	ds_read_b128 v[182:185], v202 offset:3072
	s_waitcnt lgkmcnt(0)
	v_mfma_f32_32x32x16_bf16 v[130:145], v[98:101], v[182:185], v[130:145]
	v_exp_f32_e32 v98, v102
	v_exp_f32_e32 v102, v111
	v_exp_f32_e32 v111, v112
	v_exp_f32_e32 v112, v113
	v_exp_f32_e32 v113, v12
	v_add_f32_e32 v12, 0, v82
	v_add_f32_e32 v12, v83, v12
	v_add_f32_e32 v12, v84, v12
	v_add_f32_e32 v12, v85, v12
	v_add_f32_e32 v12, v86, v12
	v_add_f32_e32 v12, v87, v12
	v_add_f32_e32 v12, v88, v12
	v_add_f32_e32 v12, v89, v12
	v_add_f32_e32 v12, v90, v12
	v_add_f32_e32 v12, v91, v12
	v_add_f32_e32 v12, v92, v12
	v_add_f32_e32 v12, v93, v12
	v_add_f32_e32 v12, v94, v12
	v_exp_f32_e32 v99, v103
	v_add_f32_e32 v12, v95, v12
	v_exp_f32_e32 v100, v104
	v_add_f32_e32 v12, v96, v12
	v_exp_f32_e32 v101, v110
	v_add_f32_e32 v12, v97, v12
	v_add_f32_e32 v12, v98, v12
	v_exp_f32_e32 v103, v14
	v_add_f32_e32 v12, v99, v12
	v_exp_f32_e32 v104, v15
	v_add_f32_e32 v12, v100, v12
	v_add_f32_e32 v12, v101, v12
	v_add_f32_e32 v12, v102, v12
	v_add_f32_e32 v12, v103, v12
	v_add_f32_e32 v12, v104, v12
	v_add_f32_e32 v12, v105, v12
	v_exp_f32_e32 v110, v13
	v_add_f32_e32 v12, v106, v12
	v_add_f32_e32 v12, v107, v12
	v_mfma_f32_32x32x16_bf16 v[114:129], v[178:181], v[182:185], v[114:129]
	v_add_f32_e32 v12, v108, v12
	v_add_f32_e32 v12, v109, v12
	v_add_f32_e32 v12, v110, v12
	v_add_f32_e32 v12, v111, v12
	v_add_f32_e32 v12, v112, v12
	v_add_f32_e32 v229, v113, v12
	v_mov_b32_e32 v230, v229
	v_cvt_pk_bf16_f32 v12, v82, v83
	v_cvt_pk_bf16_f32 v13, v84, v85
	v_cvt_pk_bf16_f32 v14, v86, v87
	v_cvt_pk_bf16_f32 v15, v88, v89
	v_cvt_pk_bf16_f32 v178, v90, v91
	v_cvt_pk_bf16_f32 v179, v92, v93
	v_cvt_pk_bf16_f32 v180, v94, v95
	v_cvt_pk_bf16_f32 v181, v96, v97
	v_cvt_pk_bf16_f32 v182, v98, v99
	v_cvt_pk_bf16_f32 v183, v100, v101
	v_cvt_pk_bf16_f32 v184, v102, v103
	v_cvt_pk_bf16_f32 v185, v104, v105
	v_cvt_pk_bf16_f32 v186, v106, v107
	v_cvt_pk_bf16_f32 v187, v108, v109
	v_cvt_pk_bf16_f32 v188, v110, v111
	v_cvt_pk_bf16_f32 v189, v112, v113
	s_nop 1
	v_permlane32_swap_b32_e32 v229, v230
	v_permlane32_swap_b32_e32 v12, v14
	v_permlane32_swap_b32_e32 v13, v15
	v_permlane32_swap_b32_e32 v178, v180
	v_permlane32_swap_b32_e32 v179, v181
	v_permlane32_swap_b32_e32 v182, v184
	v_permlane32_swap_b32_e32 v183, v185
	v_permlane32_swap_b32_e32 v186, v188
	v_permlane32_swap_b32_e32 v187, v189
	s_add_i32 s6, s36, 1
	s_cmp_lt_i32 s6, s71
	s_cselect_b64 s[50:51], -1, 0
	s_cmp_ge_i32 s6, s71
	s_cbranch_scc1 .LBB0_533
	s_sub_i32 s6, s48, 32
	s_mov_b32 s7, s11
	s_mov_b32 s49, s11
	s_lshl_b64 s[72:73], s[6:7], 12
	s_lshl_b64 s[74:75], s[48:49], 12
	v_lshl_add_u64 v[4:5], v[196:197], 0, s[72:73]
	v_lshl_add_u64 v[8:9], v[196:197], 0, s[74:75]
	v_lshl_add_u64 v[232:233], v[198:199], 0, s[72:73]
	s_add_i32 m0, s37, 0xc000
	global_load_dwordx4 v[4:7], v[4:5], off
	s_nop 0
	global_load_dwordx4 v[8:11], v[8:9], off
	s_lshl_b64 s[6:7], s[6:7], 7
	global_load_lds_dwordx4 v[232:233], off
	v_lshl_add_u64 v[232:233], v[198:199], 0, s[74:75]
	s_add_i32 m0, s37, 0xe000
	s_nop 0
	global_load_lds_dwordx4 v[232:233], off
	v_lshl_add_u64 v[232:233], v[16:17], 0, s[6:7]
	s_add_i32 m0, s37, 0x12800
	s_nop 0
	global_load_lds_dwordx4 v[232:233], off

; template <int MODE>
; __device__ __forceinline__ void partialSM(f32x16& p0, f32x16& p1, float& m_reg, float& mn, float& alpha) {
;     ...
;     const float mnL = -mn * C2;
; #pragma unroll
;     for (int r = 0; r < 16; ++r) p0[r] = fmaf(p0[r], C2, mnL);
; #pragma unroll
;     for (int r = 0; r < 16; ++r) p1[r] = fmaf(p1[r], C2, mnL);
; #pragma unroll
;     for (int r = 0; r < 16; ++r) p0[r] = __builtin_amdgcn_exp2f(p0[r]);
; }
; template <int KB, bool SK, bool ROPE, bool QHALF>
; __device__ __forceinline__ void qkt(f32x16& p0, f32x16& p1, const char* lds, int r32, int hi, const bf16x8* qr, const char* qrl, bool act) {
;     ...
;     const char* kb[4];
; #pragma unroll
;     for (int dd = 0; dd < 4; ++dd) kb[dd] = lds + OFF_K + KB * SHM_K + KSWZ(r32, (dd * 16 + hi * 8) * 2);
; #pragma unroll
;     for (int d0 = 0; d0 < 8; ++d0) { const char* a = kb[d0 & 3] + (d0 >> 2) * 128;
;         bf16x8 b0 = *reinterpret_cast<const bf16x8*>(a);
;         bf16x8 b1 = *reinterpret_cast<const bf16x8*>(a + 32 * 256);
;         bf16x8 qf;
;         if constexpr (QHALF) { if (d0 >= 4) qf = *reinterpret_cast<const bf16x8*>(qrl + (d0 - 4) * 1024); else qf = qr[d0]; } else qf = qr[d0];
;         p0 = __builtin_amdgcn_mfma_f32_32x32x16_bf16(b0, qf, p0, 0, 0, 0);
;         p1 = __builtin_amdgcn_mfma_f32_32x32x16_bf16(b1, qf, p1, 0, 0, 0); }
;     if constexpr (ROPE) {
; #pragma unroll
;         for (int d0 = 0; d0 < 4; ++d0) { const char* a = lds + OFF_KR + KB * SHM_KR + KRSWZ(r32, 2 * d0 + hi);
;             bf16x8 b0 = *reinterpret_cast<const bf16x8*>(a);
;             bf16x8 b1 = *reinterpret_cast<const bf16x8*>(a + 32 * 128);
;             const bf16x8 qf = *reinterpret_cast<const bf16x8*>(qrl + d0 * 1024);
;             p0 = __builtin_amdgcn_mfma_f32_32x32x16_bf16(b0, qf, p0, 0, 0, 0);
;             p1 = __builtin_amdgcn_mfma_f32_32x32x16_bf16(b1, qf, p1, 0, 0, 0); }
.LBB0_1035:
	v_cndmask_b32_e64 v178, v5, v227, s[6:7]
	v_mul_f32_e32 v6, 0xbdd53b94, v178
	v_fmamk_f32 v13, v137, 0x3dd53b94, v6
	v_fmamk_f32 v137, v141, 0x3dd53b94, v6
	v_mov_b32_e32 v141, v6
	v_fmamk_f32 v5, v130, 0x3dd53b94, v6
	v_fmamk_f32 v7, v131, 0x3dd53b94, v6
	v_fmamk_f32 v8, v132, 0x3dd53b94, v6
	v_fmamk_f32 v9, v133, 0x3dd53b94, v6
	v_fmamk_f32 v10, v134, 0x3dd53b94, v6
	v_fmamk_f32 v11, v135, 0x3dd53b94, v6
	v_fmamk_f32 v12, v136, 0x3dd53b94, v6
	v_fmamk_f32 v14, v138, 0x3dd53b94, v6
	v_fmamk_f32 v15, v139, 0x3dd53b94, v6
	v_fmamk_f32 v136, v140, 0x3dd53b94, v6
	v_fmamk_f32 v138, v142, 0x3dd53b94, v6
	v_fmamk_f32 v139, v143, 0x3dd53b94, v6
	v_fmamk_f32 v140, v144, 0x3dd53b94, v6
	v_fmac_f32_e32 v141, 0x3dd53b94, v145
	v_exp_f32_e32 v188, v5
	v_exp_f32_e32 v227, v7
	v_exp_f32_e32 v186, v8
	v_exp_f32_e32 v189, v9
	v_exp_f32_e32 v185, v10
	v_exp_f32_e32 v187, v11
	v_exp_f32_e32 v183, v12
	v_exp_f32_e32 v184, v13
	v_exp_f32_e32 v179, v14
	v_exp_f32_e32 v182, v15
	v_exp_f32_e32 v144, v136
	v_exp_f32_e32 v180, v137
	v_exp_f32_e32 v142, v138
	v_exp_f32_e32 v181, v139
	v_exp_f32_e32 v143, v140
	v_exp_f32_e32 v145, v141
	v_add_f32_e32 v5, v195, v225
	v_fmac_f32_e32 v5, v220, v191
	v_add_f32_e32 v191, v228, v229
	s_addk_i32 s42, 0x80
	s_add_i32 s36, s36, 2
	v_pk_fma_f32 v[128:129], v[128:129], s[14:15], v[6:7] op_sel_hi:[1,0,0]
	v_pk_fma_f32 v[126:127], v[126:127], s[14:15], v[6:7] op_sel_hi:[1,0,0]
	v_pk_fma_f32 v[130:131], v[124:125], s[14:15], v[6:7] op_sel_hi:[1,0,0]
	v_pk_fma_f32 v[132:133], v[122:123], s[14:15], v[6:7] op_sel_hi:[1,0,0]
	v_pk_fma_f32 v[134:135], v[120:121], s[14:15], v[6:7] op_sel_hi:[1,0,0]
	v_pk_fma_f32 v[136:137], v[118:119], s[14:15], v[6:7] op_sel_hi:[1,0,0]
	v_pk_fma_f32 v[138:139], v[116:117], s[14:15], v[6:7] op_sel_hi:[1,0,0]
	v_pk_fma_f32 v[140:141], v[114:115], s[14:15], v[6:7] op_sel_hi:[1,0,0]
	v_fmac_f32_e32 v191, v5, v226
	s_cmp_ge_i32 s36, s63
	v_add_u32_e32 v193, 0xffffff80, v193
	v_mov_b32_e32 v220, v4
	s_waitcnt lgkmcnt(0)
	s_cbranch_scc0 .Lmy_nobar_1
	s_barrier
	s_branch .LBB0_1052
.Lmy_nobar_1:
.LBB0_1036:
	ds_read_b128 v[4:7], v212 offset:49152
	ds_read_b128 v[8:11], v212 offset:57344
	s_add_i32 s10, 0, 0x12800
	v_exp_f32_e32 v122, v132
	v_exp_f32_e32 v123, v133
	s_waitcnt lgkmcnt(1)
	v_mfma_f32_32x32x16_bf16 v[102:117], v[4:7], v[174:177], 0
	v_exp_f32_e32 v124, v130
	v_exp_f32_e32 v125, v131
	v_exp_f32_e32 v126, v126
	v_exp_f32_e32 v127, v127
	v_exp_f32_e32 v128, v128
	v_exp_f32_e32 v129, v129
	s_add_i32 s6, s42, 0xffffff60
	s_waitcnt lgkmcnt(0)
	v_mfma_f32_32x32x16_bf16 v[86:101], v[8:11], v[174:177], 0
	ds_read_b128 v[4:7], v213 offset:49152
	ds_read_b128 v[8:11], v213 offset:57344
	s_add_i32 s7, s42, 0xffffff9f
	s_waitcnt lgkmcnt(1)
	v_mfma_f32_32x32x16_bf16 v[102:117], v[4:7], v[170:173], v[102:117]
	s_waitcnt lgkmcnt(0)
	v_mfma_f32_32x32x16_bf16 v[86:101], v[8:11], v[170:173], v[86:101]
	ds_read_b128 v[4:7], v214 offset:49152
	ds_read_b128 v[8:11], v214 offset:57344
	s_waitcnt lgkmcnt(1)
	v_mfma_f32_32x32x16_bf16 v[102:117], v[4:7], v[166:169], v[102:117]
	s_waitcnt lgkmcnt(0)
	v_mfma_f32_32x32x16_bf16 v[86:101], v[8:11], v[166:169], v[86:101]
	ds_read_b128 v[4:7], v215 offset:49152
	ds_read_b128 v[8:11], v215 offset:57344
	s_waitcnt lgkmcnt(1)
	v_mfma_f32_32x32x16_bf16 v[102:117], v[4:7], v[162:165], v[102:117]
	s_waitcnt lgkmcnt(0)
	v_mfma_f32_32x32x16_bf16 v[86:101], v[8:11], v[162:165], v[86:101]
	ds_read_b128 v[4:7], v212 offset:49280
	ds_read_b128 v[8:11], v212 offset:57472
	s_waitcnt lgkmcnt(1)
	v_mfma_f32_32x32x16_bf16 v[102:117], v[4:7], v[158:161], v[102:117]
	s_waitcnt lgkmcnt(0)
	v_mfma_f32_32x32x16_bf16 v[86:101], v[8:11], v[158:161], v[86:101]
	ds_read_b128 v[4:7], v213 offset:49280
	ds_read_b128 v[8:11], v213 offset:57472
	s_waitcnt lgkmcnt(1)
	v_mfma_f32_32x32x16_bf16 v[102:117], v[4:7], v[154:157], v[102:117]
	s_waitcnt lgkmcnt(0)
	v_mfma_f32_32x32x16_bf16 v[86:101], v[8:11], v[154:157], v[86:101]
	ds_read_b128 v[4:7], v214 offset:49280
	ds_read_b128 v[8:11], v214 offset:57472
	s_waitcnt lgkmcnt(1)
	v_mfma_f32_32x32x16_bf16 v[102:117], v[4:7], v[150:153], v[102:117]
	s_waitcnt lgkmcnt(0)
	v_mfma_f32_32x32x16_bf16 v[86:101], v[8:11], v[150:153], v[86:101]
	ds_read_b128 v[4:7], v215 offset:49280
	ds_read_b128 v[8:11], v215 offset:57472
	s_waitcnt lgkmcnt(1)
	v_mfma_f32_32x32x16_bf16 v[102:117], v[4:7], v[146:149], v[102:117]
	s_waitcnt lgkmcnt(0)
	v_mfma_f32_32x32x16_bf16 v[86:101], v[8:11], v[146:149], v[86:101]
	v_add_u32_e32 v8, s10, v216
	ds_read_b128 v[4:7], v8
	ds_read_b128 v[8:11], v8 offset:4096
	ds_read_b128 v[12:15], v202
	s_waitcnt lgkmcnt(0)
	v_mfma_f32_32x32x16_bf16 v[102:117], v[4:7], v[12:15], v[102:117]
	v_mfma_f32_32x32x16_bf16 v[86:101], v[8:11], v[12:15], v[86:101]
	v_add_u32_e32 v8, s10, v217
	ds_read_b128 v[4:7], v8
	ds_read_b128 v[8:11], v8 offset:4096
	ds_read_b128 v[12:15], v202 offset:1024
	s_waitcnt lgkmcnt(0)
	v_mfma_f32_32x32x16_bf16 v[102:117], v[4:7], v[12:15], v[102:117]
	v_mfma_f32_32x32x16_bf16 v[86:101], v[8:11], v[12:15], v[86:101]
	v_add_u32_e32 v8, s10, v218
	ds_read_b128 v[4:7], v8
	ds_read_b128 v[8:11], v8 offset:4096
	ds_read_b128 v[12:15], v202 offset:2048
	s_waitcnt lgkmcnt(0)
	v_mfma_f32_32x32x16_bf16 v[102:117], v[4:7], v[12:15], v[102:117]
	v_mfma_f32_32x32x16_bf16 v[86:101], v[8:11], v[12:15], v[86:101]
	v_add_u32_e32 v8, s10, v219
	ds_read_b128 v[4:7], v8
	ds_read_b128 v[8:11], v8 offset:4096
	ds_read_b128 v[12:15], v202 offset:3072
	s_waitcnt lgkmcnt(0)
; __device__ __forceinline__ void finishSM(f32x16& p0, f32x16& p1, float alpha, float& l_reg, bf16x8& pa0, bf16x8& pa1, bf16x8& pa2, bf16x8& pa3) {
; #pragma unroll
;     for (int r = 0; r < 16; ++r) p1[r] = __builtin_amdgcn_exp2f(p1[r]);
;     float ps = 0;
; #pragma unroll
;     for (int r = 0; r < 16; ++r) ps += p0[r];
; #pragma unroll
;     for (int r = 0; r < 16; ++r) ps += p1[r];
;     { auto rr = __builtin_amdgcn_permlane32_swap(__float_as_uint(ps), __float_as_uint(ps), false, false);
;       ps = __uint_as_float(rr[0]) + __uint_as_float(rr[1]); }
;     l_reg = l_reg * alpha + ps;
;     ...
;     PK4(p0, 0, pa0); PK4(p0, 8, pa1); PK4(p1, 0, pa2); PK4(p1, 8, pa3);
;     ...
; }
; template <int VB, bool SK>
; __device__ __forceinline__ void pv_tile(f32x16* o, int vb0, bf16x8 pa0, bf16x8 pa1, bf16x8 pa2, bf16x8 pa3, bool act) {
;     if (SK && !act) return;
;     ...
;     if (ATT_PRIO) __builtin_amdgcn_s_setprio(1);
;     PV_D0(0); PV_D0(1); PV_D0(2); PV_D0(3);
	v_mfma_f32_32x32x16_bf16 v[102:117], v[4:7], v[12:15], v[102:117]
	v_exp_f32_e32 v4, v140
	v_exp_f32_e32 v5, v141
	v_exp_f32_e32 v6, v138
	v_exp_f32_e32 v7, v139
	v_mfma_f32_32x32x16_bf16 v[86:101], v[8:11], v[12:15], v[86:101]
	v_add_f32_e32 v12, 0, v188
	v_add_f32_e32 v12, v227, v12
	v_add_f32_e32 v12, v186, v12
	v_add_f32_e32 v12, v189, v12
	v_add_f32_e32 v12, v185, v12
	v_add_f32_e32 v12, v187, v12
	v_add_f32_e32 v12, v183, v12
	v_add_f32_e32 v12, v184, v12
	v_add_f32_e32 v12, v179, v12
	v_add_f32_e32 v12, v182, v12
	v_add_f32_e32 v12, v144, v12
	v_add_f32_e32 v12, v180, v12
	v_add_f32_e32 v12, v142, v12
	v_add_f32_e32 v12, v181, v12
	v_add_f32_e32 v12, v143, v12
	v_add_f32_e32 v12, v145, v12
	v_exp_f32_e32 v8, v136
	v_add_f32_e32 v12, v4, v12
	v_exp_f32_e32 v9, v137
	v_add_f32_e32 v12, v5, v12
	v_exp_f32_e32 v10, v134
	v_add_f32_e32 v12, v6, v12
	v_exp_f32_e32 v11, v135
	v_add_f32_e32 v12, v7, v12
	v_add_f32_e32 v12, v8, v12
	v_add_f32_e32 v12, v9, v12
	v_add_f32_e32 v12, v10, v12
	v_add_f32_e32 v12, v11, v12
	v_add_f32_e32 v12, v122, v12
	v_add_f32_e32 v12, v123, v12
	v_add_f32_e32 v12, v124, v12
	v_add_f32_e32 v12, v125, v12
	v_add_f32_e32 v12, v126, v12
	v_add_f32_e32 v12, v127, v12
	v_add_f32_e32 v12, v128, v12
	v_add_f32_e32 v195, v129, v12
	v_mov_b32_e32 v225, v195
	s_nop 1
	v_permlane32_swap_b32_e32 v195, v225
	v_cvt_pk_bf16_f32 v12, v188, v227
	v_cvt_pk_bf16_f32 v13, v186, v189
	v_cvt_pk_bf16_f32 v14, v185, v187
	v_cvt_pk_bf16_f32 v15, v183, v184
	v_cvt_pk_bf16_f32 v82, v179, v182
	v_cvt_pk_bf16_f32 v83, v144, v180
	v_cvt_pk_bf16_f32 v84, v142, v181
	v_cvt_pk_bf16_f32 v85, v143, v145
	v_cvt_pk_bf16_f32 v118, v4, v5
	v_cvt_pk_bf16_f32 v119, v6, v7
	v_cvt_pk_bf16_f32 v120, v8, v9
	v_cvt_pk_bf16_f32 v121, v10, v11
	v_cvt_pk_bf16_f32 v122, v122, v123
	v_cvt_pk_bf16_f32 v123, v124, v125
	v_cvt_pk_bf16_f32 v124, v126, v127
	v_cvt_pk_bf16_f32 v125, v128, v129
	s_nop 0
	v_permlane32_swap_b32_e32 v12, v14
	v_permlane32_swap_b32_e32 v13, v15
	v_permlane32_swap_b32_e32 v82, v84
	v_permlane32_swap_b32_e32 v83, v85
	v_permlane32_swap_b32_e32 v118, v120
	v_permlane32_swap_b32_e32 v119, v121
	v_permlane32_swap_b32_e32 v122, v124
	v_permlane32_swap_b32_e32 v123, v125
	s_add_i32 s10, s42, 0xffffffa0
	s_sub_i32 s64, s42, 64
	s_mov_b32 s65, s11
	s_lshl_b64 s[44:45], s[10:11], 12
	s_lshl_b64 s[64:65], s[64:65], 12
	v_lshl_add_u64 v[4:5], v[196:197], 0, s[44:45]
	v_lshl_add_u64 v[8:9], v[196:197], 0, s[64:65]
	v_lshl_add_u64 v[126:127], v[198:199], 0, s[44:45]
	s_add_i32 m0, s37, 0x8000
	global_load_dwordx4 v[4:7], v[4:5], off
	s_nop 0
	global_load_dwordx4 v[8:11], v[8:9], off
	s_lshl_b64 s[44:45], s[10:11], 7
	global_load_lds_dwordx4 v[126:127], off
	v_lshl_add_u64 v[126:127], v[198:199], 0, s[64:65]
	s_add_i32 m0, s37, 0xa000
	s_nop 0
	global_load_lds_dwordx4 v[126:127], off
	v_lshl_add_u64 v[126:127], v[16:17], 0, s[44:45]
	s_add_i32 m0, s37, 0x10800
	s_nop 0
	global_load_lds_dwordx4 v[126:127], off
	ds_read_b64_tr_b16 v[126:127], v209 offset:0
	ds_read_b64_tr_b16 v[128:129], v209 offset:0x800
	ds_read_b64_tr_b16 v[130:131], v209 offset:0x1000
	ds_read_b64_tr_b16 v[132:133], v209 offset:0x1800
	ds_read_b64_tr_b16 v[134:135], v209 offset:0x2000
	ds_read_b64_tr_b16 v[136:137], v209 offset:0x2800
	ds_read_b64_tr_b16 v[138:139], v209 offset:0x3000
	ds_read_b64_tr_b16 v[140:141], v209 offset:0x3800
	s_waitcnt lgkmcnt(0)
	s_nop 0
	v_mfma_f32_32x32x16_bf16 v[66:81], v[12:15], v[126:129], v[66:81]
	ds_read_b64_tr_b16 v[126:127], v209 offset:0x200
	ds_read_b64_tr_b16 v[128:129], v209 offset:0xa00
	v_mfma_f32_32x32x16_bf16 v[66:81], v[82:85], v[130:133], v[66:81]
	ds_read_b64_tr_b16 v[130:131], v209 offset:0x1200
	ds_read_b64_tr_b16 v[132:133], v209 offset:0x1a00
	v_mfma_f32_32x32x16_bf16 v[66:81], v[118:121], v[134:137], v[66:81]
	ds_read_b64_tr_b16 v[134:135], v209 offset:0x2200
	ds_read_b64_tr_b16 v[136:137], v209 offset:0x2a00
	ds_read_b64_tr_b16 v[142:143], v209 offset:0x3200
	ds_read_b64_tr_b16 v[144:145], v209 offset:0x3a00
	s_waitcnt lgkmcnt(0)
	v_mfma_f32_32x32x16_bf16 v[66:81], v[122:125], v[138:141], v[66:81]
	v_mfma_f32_32x32x16_bf16 v[50:65], v[12:15], v[126:129], v[50:65]
	ds_read_b64_tr_b16 v[126:127], v209 offset:0x400
	ds_read_b64_tr_b16 v[128:129], v209 offset:0xc00
	v_mfma_f32_32x32x16_bf16 v[50:65], v[82:85], v[130:133], v[50:65]
	ds_read_b64_tr_b16 v[130:131], v209 offset:0x1400
	ds_read_b64_tr_b16 v[132:133], v209 offset:0x1c00
	v_mfma_f32_32x32x16_bf16 v[50:65], v[118:121], v[134:137], v[50:65]
	ds_read_b64_tr_b16 v[134:135], v209 offset:0x2400
	ds_read_b64_tr_b16 v[136:137], v209 offset:0x2c00
	ds_read_b64_tr_b16 v[138:139], v209 offset:0x3400
	ds_read_b64_tr_b16 v[140:141], v209 offset:0x3c00
	s_waitcnt lgkmcnt(0)
	v_mfma_f32_32x32x16_bf16 v[50:65], v[122:125], v[142:145], v[50:65]
	v_mfma_f32_32x32x16_bf16 v[34:49], v[12:15], v[126:129], v[34:49]
	ds_read_b64_tr_b16 v[126:127], v209 offset:0x600
	ds_read_b64_tr_b16 v[128:129], v209 offset:0xe00
	v_mfma_f32_32x32x16_bf16 v[34:49], v[82:85], v[130:133], v[34:49]
	ds_read_b64_tr_b16 v[130:131], v209 offset:0x1600
	ds_read_b64_tr_b16 v[132:133], v209 offset:0x1e00
	v_mfma_f32_32x32x16_bf16 v[34:49], v[118:121], v[134:137], v[34:49]
	ds_read_b64_tr_b16 v[134:135], v209 offset:0x2600
	ds_read_b64_tr_b16 v[136:137], v209 offset:0x2e00
	ds_read_b64_tr_b16 v[142:143], v209 offset:0x3600
	ds_read_b64_tr_b16 v[144:145], v209 offset:0x3e00
	s_waitcnt lgkmcnt(0)
	v_mfma_f32_32x32x16_bf16 v[34:49], v[122:125], v[138:141], v[34:49]
	v_mfma_f32_32x32x16_bf16 v[18:33], v[12:15], v[126:129], v[18:33]
	s_cmp_le_i32 s7, s40
	s_cselect_b64 s[44:45], -1, 0
	s_cmp_gt_i32 s6, s60
	s_cselect_b64 s[6:7], -1, 0
	s_and_b64 s[6:7], s[6:7], s[44:45]
	s_and_b64 vcc, exec, s[6:7]
	v_mfma_f32_32x32x16_bf16 v[18:33], v[82:85], v[130:133], v[18:33]
	v_mfma_f32_32x32x16_bf16 v[18:33], v[118:121], v[134:137], v[18:33]
	v_mfma_f32_32x32x16_bf16 v[18:33], v[122:125], v[142:145], v[18:33]
	s_cbranch_vccnz .LBB0_1038
; __device__ __forceinline__ void mask_tile(f32x16& p0, f32x16& p1, int dq, unsigned W) {
;     const float NEG = -__builtin_inff();
; #pragma unroll
;     for (int r = 0; r < 16; ++r) {
;         const int c = (r & 3) + 8 * (r >> 2);
;         if ((unsigned)(dq - c) >= W) p0[r] = NEG;
;         if ((unsigned)(dq - c - 32) >= W) p1[r] = NEG;
;     }
; }
	v_add_u32_e32 v12, 0x7b, v193
	v_cmp_gt_u32_e32 vcc, 2.0, v12
	v_add_u32_e32 v12, 0x5b, v193
	s_nop 0
	v_cndmask_b32_e32 v102, v200, v102, vcc
	v_cmp_gt_u32_e32 vcc, 2.0, v12
	v_add_u32_e32 v12, 0x7a, v193
	s_nop 0
	v_cndmask_b32_e32 v86, v200, v86, vcc
	v_cmp_gt_u32_e32 vcc, 2.0, v12
	v_add_u32_e32 v12, 0x5a, v193
	s_nop 0
	v_cndmask_b32_e32 v103, v200, v103, vcc
	v_cmp_gt_u32_e32 vcc, 2.0, v12
	v_add_u32_e32 v12, 0x79, v193
	s_nop 0
	v_cndmask_b32_e32 v87, v200, v87, vcc
	v_cmp_gt_u32_e32 vcc, 2.0, v12
	v_add_u32_e32 v12, 0x59, v193
	s_nop 0
	v_cndmask_b32_e32 v104, v200, v104, vcc
	v_cmp_gt_u32_e32 vcc, 2.0, v12
	v_add_u32_e32 v12, 0x78, v193
	s_nop 0
	v_cndmask_b32_e32 v88, v200, v88, vcc
	v_cmp_gt_u32_e32 vcc, 2.0, v12
	v_add_u32_e32 v12, 0x58, v193
	s_nop 0
	v_cndmask_b32_e32 v105, v200, v105, vcc
	v_cmp_gt_u32_e32 vcc, 2.0, v12
	v_add_u32_e32 v12, 0x73, v193
	s_nop 0
	v_cndmask_b32_e32 v89, v200, v89, vcc
	v_cmp_gt_u32_e32 vcc, 2.0, v12
	v_add_u32_e32 v12, 0x53, v193
	s_nop 0
	v_cndmask_b32_e32 v106, v200, v106, vcc
	v_cmp_gt_u32_e32 vcc, 2.0, v12
	v_add_u32_e32 v12, 0x72, v193
	s_nop 0
	v_cndmask_b32_e32 v90, v200, v90, vcc
	v_cmp_gt_u32_e32 vcc, 2.0, v12
	v_add_u32_e32 v12, 0x52, v193
	s_nop 0
	v_cndmask_b32_e32 v107, v200, v107, vcc
	v_cmp_gt_u32_e32 vcc, 2.0, v12
	v_add_u32_e32 v12, 0x71, v193
	s_nop 0
	v_cndmask_b32_e32 v91, v200, v91, vcc
	v_cmp_gt_u32_e32 vcc, 2.0, v12
	v_add_u32_e32 v12, 0x51, v193
	s_nop 0
	v_cndmask_b32_e32 v108, v200, v108, vcc
	v_cmp_gt_u32_e32 vcc, 2.0, v12
	v_add_u32_e32 v12, 0x70, v193
	s_nop 0
	v_cndmask_b32_e32 v92, v200, v92, vcc
	v_cmp_gt_u32_e32 vcc, 2.0, v12
	v_add_u32_e32 v12, 0x50, v193
	s_nop 0
	v_cndmask_b32_e32 v109, v200, v109, vcc
	v_cmp_gt_u32_e32 vcc, 2.0, v12
	v_add_u32_e32 v12, 0x6b, v193
	s_nop 0
	v_cndmask_b32_e32 v93, v200, v93, vcc
	v_cmp_gt_u32_e32 vcc, 2.0, v12
	v_add_u32_e32 v12, 0x4b, v193
	s_nop 0
	v_cndmask_b32_e32 v110, v200, v110, vcc
	v_cmp_gt_u32_e32 vcc, 2.0, v12
	v_add_u32_e32 v12, 0x6a, v193
	s_nop 0
	v_cndmask_b32_e32 v94, v200, v94, vcc
	v_cmp_gt_u32_e32 vcc, 2.0, v12
	v_add_u32_e32 v12, 0x4a, v193
	s_nop 0
	v_cndmask_b32_e32 v111, v200, v111, vcc
	v_cmp_gt_u32_e32 vcc, 2.0, v12
	v_add_u32_e32 v12, 0x69, v193
	s_nop 0
	v_cndmask_b32_e32 v95, v200, v95, vcc
	v_cmp_gt_u32_e32 vcc, 2.0, v12
	v_add_u32_e32 v12, 0x49, v193
	s_nop 0
	v_cndmask_b32_e32 v112, v200, v112, vcc
	v_cmp_gt_u32_e32 vcc, 2.0, v12
	v_add_u32_e32 v12, 0x68, v193
	s_nop 0
	v_cndmask_b32_e32 v96, v200, v96, vcc
	v_cmp_gt_u32_e32 vcc, 2.0, v12
	v_add_u32_e32 v12, 0x48, v193
	s_nop 0
	v_cndmask_b32_e32 v113, v200, v113, vcc
	v_cmp_gt_u32_e32 vcc, 2.0, v12
	v_add_u32_e32 v12, 0x63, v193
	s_nop 0
	v_cndmask_b32_e32 v97, v200, v97, vcc
	v_cmp_gt_u32_e32 vcc, 2.0, v12
	v_add_u32_e32 v12, 0x43, v193
	s_nop 0
	v_cndmask_b32_e32 v114, v200, v114, vcc
	v_cmp_gt_u32_e32 vcc, 2.0, v12
	v_add_u32_e32 v12, 0x62, v193
	s_nop 0
	v_cndmask_b32_e32 v98, v200, v98, vcc
	v_cmp_gt_u32_e32 vcc, 2.0, v12
	v_add_u32_e32 v12, 0x42, v193
	s_nop 0
	v_cndmask_b32_e32 v115, v200, v115, vcc
	v_cmp_gt_u32_e32 vcc, 2.0, v12
	v_add_u32_e32 v12, 0x61, v193
	s_nop 0
	v_cndmask_b32_e32 v99, v200, v99, vcc
	v_cmp_gt_u32_e32 vcc, 2.0, v12
	v_add_u32_e32 v12, 0x41, v193
	s_nop 0
	v_cndmask_b32_e32 v116, v200, v116, vcc
	v_cmp_gt_u32_e32 vcc, 2.0, v12
	v_add_u32_e32 v12, 0x60, v193
	s_nop 0
	v_cndmask_b32_e32 v100, v200, v100, vcc
	v_cmp_gt_u32_e32 vcc, 2.0, v12
	v_add_u32_e32 v12, 64, v193
	s_nop 0
	v_cndmask_b32_e32 v117, v200, v117, vcc
	v_cmp_gt_u32_e32 vcc, 2.0, v12
	s_nop 1
	v_cndmask_b32_e32 v101, v200, v101, vcc

; template <int MODE>
; __device__ __forceinline__ void partialSM(f32x16& p0, f32x16& p1, float& m_reg, float& mn, float& alpha) {
;     ...
;     constexpr float C2 = 1.4426950408889634f * SCALE;
;     if (__builtin_expect(__all((pmax - m_reg) * SCALE <= THR), 1)) { mn = m_reg; alpha = 1.f; }
;     else { mn = fmaxf(m_reg, pmax); alpha = __builtin_amdgcn_exp2f((m_reg - mn) * C2); m_reg = mn; }
;     const float mnL = -mn * C2;
; #pragma unroll
;     for (int r = 0; r < 16; ++r) p0[r] = fmaf(p0[r], C2, mnL);
; #pragma unroll
;     for (int r = 0; r < 16; ++r) p1[r] = fmaf(p1[r], C2, mnL);
; #pragma unroll
;     for (int r = 0; r < 16; ++r) p0[r] = __builtin_amdgcn_exp2f(p0[r]);
; template <int KB, bool SK, bool ROPE, bool QHALF>
; __device__ __forceinline__ void qkt(f32x16& p0, f32x16& p1, const char* lds, int r32, int hi, const bf16x8* qr, const char* qrl, bool act) {
;     ...
;     const char* kb[4];
; #pragma unroll
;     for (int dd = 0; dd < 4; ++dd) kb[dd] = lds + OFF_K + KB * SHM_K + KSWZ(r32, (dd * 16 + hi * 8) * 2);
; #pragma unroll
;     for (int d0 = 0; d0 < 8; ++d0) { const char* a = kb[d0 & 3] + (d0 >> 2) * 128;
;         bf16x8 b0 = *reinterpret_cast<const bf16x8*>(a);
;         bf16x8 b1 = *reinterpret_cast<const bf16x8*>(a + 32 * 256);
;         bf16x8 qf;
;         if constexpr (QHALF) { if (d0 >= 4) qf = *reinterpret_cast<const bf16x8*>(qrl + (d0 - 4) * 1024); else qf = qr[d0]; } else qf = qr[d0];
;         p0 = __builtin_amdgcn_mfma_f32_32x32x16_bf16(b0, qf, p0, 0, 0, 0);
;         p1 = __builtin_amdgcn_mfma_f32_32x32x16_bf16(b1, qf, p1, 0, 0, 0); }
.LBB0_1042:
	v_cndmask_b32_e64 v227, v12, v178, s[6:7]
	v_mul_f32_e32 v12, 0xbdd53b94, v227
	v_fmamk_f32 v82, v102, 0x3dd53b94, v12
	v_fmamk_f32 v83, v103, 0x3dd53b94, v12
	v_fmamk_f32 v84, v104, 0x3dd53b94, v12
	v_fmamk_f32 v85, v105, 0x3dd53b94, v12
	v_fmamk_f32 v118, v106, 0x3dd53b94, v12
	v_fmamk_f32 v119, v107, 0x3dd53b94, v12
	v_fmamk_f32 v120, v108, 0x3dd53b94, v12
	v_fmamk_f32 v121, v109, 0x3dd53b94, v12
	v_fmamk_f32 v122, v110, 0x3dd53b94, v12
	v_fmamk_f32 v123, v111, 0x3dd53b94, v12
	v_fmamk_f32 v112, v112, 0x3dd53b94, v12
	v_fmamk_f32 v113, v113, 0x3dd53b94, v12
	v_fmamk_f32 v114, v114, 0x3dd53b94, v12
	v_fmamk_f32 v115, v115, 0x3dd53b94, v12
	v_fmamk_f32 v116, v116, 0x3dd53b94, v12
	v_fmamk_f32 v117, v117, 0x3dd53b94, v12
	v_fmamk_f32 v102, v86, 0x3dd53b94, v12
	v_fmamk_f32 v103, v87, 0x3dd53b94, v12
	v_fmamk_f32 v104, v88, 0x3dd53b94, v12
	v_fmamk_f32 v110, v89, 0x3dd53b94, v12
	v_fmamk_f32 v111, v90, 0x3dd53b94, v12
	v_fmamk_f32 v14, v91, 0x3dd53b94, v12
	v_fmamk_f32 v15, v92, 0x3dd53b94, v12
	v_fmamk_f32 v105, v93, 0x3dd53b94, v12
	v_fmamk_f32 v106, v94, 0x3dd53b94, v12
	v_fmamk_f32 v107, v95, 0x3dd53b94, v12
	v_fmamk_f32 v108, v96, 0x3dd53b94, v12
	v_fmamk_f32 v109, v97, 0x3dd53b94, v12
	v_exp_f32_e32 v82, v82
	v_exp_f32_e32 v83, v83
	v_exp_f32_e32 v84, v84
	v_exp_f32_e32 v85, v85
	v_exp_f32_e32 v86, v118
	v_exp_f32_e32 v87, v119
	v_exp_f32_e32 v88, v120
	v_exp_f32_e32 v89, v121
	v_exp_f32_e32 v90, v122
	v_exp_f32_e32 v91, v123
	v_exp_f32_e32 v92, v112
	v_exp_f32_e32 v93, v113
	v_exp_f32_e32 v94, v114
	v_exp_f32_e32 v95, v115
	v_exp_f32_e32 v96, v116
	v_exp_f32_e32 v97, v117
	v_fmamk_f32 v13, v98, 0x3dd53b94, v12
	v_fmamk_f32 v112, v99, 0x3dd53b94, v12
	v_fmamk_f32 v113, v100, 0x3dd53b94, v12
	v_fmac_f32_e32 v12, 0x3dd53b94, v101
	s_waitcnt lgkmcnt(0)
	ds_read_b128 v[98:101], v212 offset:32768
	ds_read_b128 v[114:117], v212 offset:40960
	v_exp_f32_e32 v105, v105
	v_exp_f32_e32 v106, v106
	v_exp_f32_e32 v107, v107
	s_waitcnt lgkmcnt(1)
	v_mfma_f32_32x32x16_bf16 v[130:145], v[98:101], v[174:177], 0
	ds_read_b128 v[98:101], v213 offset:32768
	ds_read_b128 v[178:181], v213 offset:40960
	v_exp_f32_e32 v108, v108
	v_exp_f32_e32 v109, v109
	s_waitcnt lgkmcnt(2)
	v_mfma_f32_32x32x16_bf16 v[114:129], v[114:117], v[174:177], 0
	s_waitcnt lgkmcnt(1)
	v_mfma_f32_32x32x16_bf16 v[130:145], v[98:101], v[170:173], v[130:145]
	s_waitcnt lgkmcnt(0)
	v_mfma_f32_32x32x16_bf16 v[114:129], v[178:181], v[170:173], v[114:129]
	ds_read_b128 v[98:101], v214 offset:32768
	ds_read_b128 v[178:181], v214 offset:40960
	s_waitcnt lgkmcnt(1)
	v_mfma_f32_32x32x16_bf16 v[130:145], v[98:101], v[166:169], v[130:145]
	s_waitcnt lgkmcnt(0)
	v_mfma_f32_32x32x16_bf16 v[114:129], v[178:181], v[166:169], v[114:129]
	ds_read_b128 v[98:101], v215 offset:32768
	ds_read_b128 v[178:181], v215 offset:40960
	s_waitcnt lgkmcnt(1)
	v_mfma_f32_32x32x16_bf16 v[130:145], v[98:101], v[162:165], v[130:145]
	s_waitcnt lgkmcnt(0)
	v_mfma_f32_32x32x16_bf16 v[114:129], v[178:181], v[162:165], v[114:129]
	ds_read_b128 v[98:101], v212 offset:32896
	ds_read_b128 v[178:181], v212 offset:41088
	s_waitcnt lgkmcnt(1)
	v_mfma_f32_32x32x16_bf16 v[130:145], v[98:101], v[158:161], v[130:145]
	s_waitcnt lgkmcnt(0)
	v_mfma_f32_32x32x16_bf16 v[114:129], v[178:181], v[158:161], v[114:129]
	ds_read_b128 v[98:101], v213 offset:32896
	ds_read_b128 v[178:181], v213 offset:41088
	s_waitcnt lgkmcnt(1)
	v_mfma_f32_32x32x16_bf16 v[130:145], v[98:101], v[154:157], v[130:145]
	s_waitcnt lgkmcnt(0)
	v_mfma_f32_32x32x16_bf16 v[114:129], v[178:181], v[154:157], v[114:129]
	ds_read_b128 v[98:101], v214 offset:32896
	ds_read_b128 v[178:181], v214 offset:41088
	s_waitcnt lgkmcnt(1)
	v_mfma_f32_32x32x16_bf16 v[130:145], v[98:101], v[150:153], v[130:145]
	s_waitcnt lgkmcnt(0)
	v_mfma_f32_32x32x16_bf16 v[114:129], v[178:181], v[150:153], v[114:129]
	ds_read_b128 v[98:101], v215 offset:32896
	ds_read_b128 v[178:181], v215 offset:41088
	s_waitcnt lgkmcnt(1)
	v_mfma_f32_32x32x16_bf16 v[130:145], v[98:101], v[146:149], v[130:145]
	s_waitcnt lgkmcnt(0)
; __device__ __forceinline__ void finishSM(f32x16& p0, f32x16& p1, float alpha, float& l_reg, bf16x8& pa0, bf16x8& pa1, bf16x8& pa2, bf16x8& pa3) {
; #pragma unroll
;     for (int r = 0; r < 16; ++r) p1[r] = __builtin_amdgcn_exp2f(p1[r]);
;     float ps = 0;
; #pragma unroll
;     for (int r = 0; r < 16; ++r) ps += p0[r];
; #pragma unroll
;     for (int r = 0; r < 16; ++r) ps += p1[r];
;     { auto rr = __builtin_amdgcn_permlane32_swap(__float_as_uint(ps), __float_as_uint(ps), false, false);
;       ps = __uint_as_float(rr[0]) + __uint_as_float(rr[1]); }
;     l_reg = l_reg * alpha + ps;
;     ...
;     PK4(p0, 0, pa0); PK4(p0, 8, pa1); PK4(p1, 0, pa2); PK4(p1, 8, pa3);
;     ...
; }
; template <int KB, bool SK, bool ROPE, bool QHALF>
; __device__ __forceinline__ void qkt(f32x16& p0, f32x16& p1, const char* lds, int r32, int hi, const bf16x8* qr, const char* qrl, bool act) {
;     ...
;     if constexpr (ROPE) {
; #pragma unroll
;         for (int d0 = 0; d0 < 4; ++d0) { const char* a = lds + OFF_KR + KB * SHM_KR + KRSWZ(r32, 2 * d0 + hi);
;             bf16x8 b0 = *reinterpret_cast<const bf16x8*>(a);
;             bf16x8 b1 = *reinterpret_cast<const bf16x8*>(a + 32 * 128);
;             const bf16x8 qf = *reinterpret_cast<const bf16x8*>(qrl + d0 * 1024);
;             p0 = __builtin_amdgcn_mfma_f32_32x32x16_bf16(b0, qf, p0, 0, 0, 0);
;             p1 = __builtin_amdgcn_mfma_f32_32x32x16_bf16(b1, qf, p1, 0, 0, 0); }
	v_mfma_f32_32x32x16_bf16 v[114:129], v[178:181], v[146:149], v[114:129]
	ds_read_b128 v[98:101], v221
	ds_read_b128 v[178:181], v221 offset:4096
	ds_read_b128 v[182:185], v202
	s_waitcnt lgkmcnt(0)
	v_mfma_f32_32x32x16_bf16 v[130:145], v[98:101], v[182:185], v[130:145]
	v_mfma_f32_32x32x16_bf16 v[114:129], v[178:181], v[182:185], v[114:129]
	ds_read_b128 v[98:101], v222
	ds_read_b128 v[178:181], v222 offset:4096
	ds_read_b128 v[182:185], v202 offset:1024
	s_waitcnt lgkmcnt(0)
	v_mfma_f32_32x32x16_bf16 v[130:145], v[98:101], v[182:185], v[130:145]
	v_mfma_f32_32x32x16_bf16 v[114:129], v[178:181], v[182:185], v[114:129]
	ds_read_b128 v[98:101], v223
	ds_read_b128 v[178:181], v223 offset:4096
	ds_read_b128 v[182:185], v202 offset:2048
	s_waitcnt lgkmcnt(0)
	v_mfma_f32_32x32x16_bf16 v[130:145], v[98:101], v[182:185], v[130:145]
	v_mfma_f32_32x32x16_bf16 v[114:129], v[178:181], v[182:185], v[114:129]
	ds_read_b128 v[98:101], v224
	ds_read_b128 v[178:181], v224 offset:4096
	ds_read_b128 v[182:185], v202 offset:3072
	s_waitcnt lgkmcnt(0)
	v_mfma_f32_32x32x16_bf16 v[130:145], v[98:101], v[182:185], v[130:145]
	v_exp_f32_e32 v98, v102
	v_exp_f32_e32 v102, v111
	v_exp_f32_e32 v111, v112
	v_exp_f32_e32 v112, v113
	v_exp_f32_e32 v113, v12
	v_add_f32_e32 v12, 0, v82
	v_add_f32_e32 v12, v83, v12
	v_add_f32_e32 v12, v84, v12
	v_add_f32_e32 v12, v85, v12
	v_add_f32_e32 v12, v86, v12
	v_add_f32_e32 v12, v87, v12
	v_add_f32_e32 v12, v88, v12
	v_add_f32_e32 v12, v89, v12
	v_add_f32_e32 v12, v90, v12
	v_add_f32_e32 v12, v91, v12
	v_add_f32_e32 v12, v92, v12
	v_add_f32_e32 v12, v93, v12
	v_add_f32_e32 v12, v94, v12
	v_exp_f32_e32 v99, v103
	v_add_f32_e32 v12, v95, v12
	v_exp_f32_e32 v100, v104
	v_add_f32_e32 v12, v96, v12
	v_exp_f32_e32 v101, v110
	v_add_f32_e32 v12, v97, v12
	v_add_f32_e32 v12, v98, v12
	v_exp_f32_e32 v103, v14
	v_add_f32_e32 v12, v99, v12
	v_exp_f32_e32 v104, v15
	v_add_f32_e32 v12, v100, v12
	v_add_f32_e32 v12, v101, v12
	v_add_f32_e32 v12, v102, v12
	v_add_f32_e32 v12, v103, v12
	v_add_f32_e32 v12, v104, v12
	v_add_f32_e32 v12, v105, v12
	v_exp_f32_e32 v110, v13
	v_add_f32_e32 v12, v106, v12
	v_add_f32_e32 v12, v107, v12
	v_mfma_f32_32x32x16_bf16 v[114:129], v[178:181], v[182:185], v[114:129]
	v_add_f32_e32 v12, v108, v12
	v_add_f32_e32 v12, v109, v12
	v_add_f32_e32 v12, v110, v12
	v_add_f32_e32 v12, v111, v12
	v_add_f32_e32 v12, v112, v12
	v_add_f32_e32 v228, v113, v12
	v_mov_b32_e32 v229, v228
	v_cvt_pk_bf16_f32 v12, v82, v83
	v_cvt_pk_bf16_f32 v13, v84, v85
	v_cvt_pk_bf16_f32 v14, v86, v87
	v_cvt_pk_bf16_f32 v15, v88, v89
	v_cvt_pk_bf16_f32 v178, v90, v91
	v_cvt_pk_bf16_f32 v179, v92, v93
	v_cvt_pk_bf16_f32 v180, v94, v95
	v_cvt_pk_bf16_f32 v181, v96, v97
	v_cvt_pk_bf16_f32 v182, v98, v99
	v_cvt_pk_bf16_f32 v183, v100, v101
	v_cvt_pk_bf16_f32 v184, v102, v103
	v_cvt_pk_bf16_f32 v185, v104, v105
	v_cvt_pk_bf16_f32 v186, v106, v107
	v_cvt_pk_bf16_f32 v187, v108, v109
	v_cvt_pk_bf16_f32 v188, v110, v111
	v_cvt_pk_bf16_f32 v189, v112, v113
	s_nop 1
	v_permlane32_swap_b32_e32 v228, v229
	v_permlane32_swap_b32_e32 v12, v14
	v_permlane32_swap_b32_e32 v13, v15
	v_permlane32_swap_b32_e32 v178, v180
	v_permlane32_swap_b32_e32 v179, v181
	v_permlane32_swap_b32_e32 v182, v184
	v_permlane32_swap_b32_e32 v183, v185
	v_permlane32_swap_b32_e32 v186, v188
	v_permlane32_swap_b32_e32 v187, v189
	s_add_i32 s6, s36, 1
	s_cmp_lt_i32 s6, s63
	s_cselect_b64 s[44:45], -1, 0
	s_cmp_ge_i32 s6, s63
	s_cbranch_scc1 .LBB0_1044
	s_sub_i32 s6, s42, 32
	s_mov_b32 s7, s11
	s_mov_b32 s43, s11
	s_lshl_b64 s[64:65], s[6:7], 12
	s_lshl_b64 s[66:67], s[42:43], 12
	v_lshl_add_u64 v[4:5], v[196:197], 0, s[64:65]
	v_lshl_add_u64 v[8:9], v[196:197], 0, s[66:67]
	v_lshl_add_u64 v[230:231], v[198:199], 0, s[64:65]
	s_add_i32 m0, s37, 0xc000
	global_load_dwordx4 v[4:7], v[4:5], off
	s_nop 0
	global_load_dwordx4 v[8:11], v[8:9], off
	s_lshl_b64 s[6:7], s[6:7], 7
	global_load_lds_dwordx4 v[230:231], off
	v_lshl_add_u64 v[230:231], v[198:199], 0, s[66:67]
	s_add_i32 m0, s37, 0xe000
	s_nop 0
	global_load_lds_dwordx4 v[230:231], off
	v_lshl_add_u64 v[230:231], v[16:17], 0, s[6:7]
	s_add_i32 m0, s37, 0x12800
	s_nop 0
	global_load_lds_dwordx4 v[230:231], off
